# P5 compact path: candidate LDS reads batched 2x12 with counted waits, plus a skipped 60-byte pad so that all later code keeps the placement (mod 64) of the previous best
# speedup vs baseline: 1.0046x; 1.0046x over previous
.LBB0_542:
	s_or_saveexec_b64 s[12:13], s[12:13]
	s_nop 0
	v_mov_b32_e32 v144, s18
	v_mov_b32_e32 v145, s17
	s_xor_b64 exec, exec, s[12:13]
	s_cbranch_execz .LBB0_546
	ds_read_b32 v144, v8 offset:8192
	ds_read_b32 v146, v8 offset:8448
	ds_read_b32 v145, v8 offset:8704
	ds_read_b32 v147, v8 offset:8960
	ds_read_b32 v149, v8 offset:9216
	ds_read_b32 v150, v8 offset:9472
	ds_read_b32 v151, v8 offset:9728
	ds_read_b32 v152, v8 offset:9984
	ds_read_b32 v153, v8 offset:10240
	ds_read_b32 v154, v8 offset:10496
	ds_read_b32 v155, v8 offset:10752
	ds_read_b32 v156, v8 offset:11008
	v_cmp_lt_u32_e32 vcc, s30, v148
	s_waitcnt lgkmcnt(11)
	s_nop 0
	v_cndmask_b32_e32 v144, 0, v144, vcc
	v_cmp_lt_u32_e32 vcc, s36, v148
	s_waitcnt lgkmcnt(10)
	s_nop 0
	v_cndmask_b32_e32 v146, 0, v146, vcc
	v_cmp_lt_u32_e32 vcc, s37, v148
	s_waitcnt lgkmcnt(9)
	s_nop 0
	v_cndmask_b32_e32 v145, 0, v145, vcc
	v_cmp_lt_u32_e32 vcc, s64, v148
	s_waitcnt lgkmcnt(8)
	s_nop 0
	v_cndmask_b32_e32 v147, 0, v147, vcc
	v_cmp_lt_u32_e32 vcc, s38, v148
	s_waitcnt lgkmcnt(7)
	s_nop 0
	v_cndmask_b32_e32 v149, 0, v149, vcc
	v_cmp_lt_u32_e32 vcc, s39, v148
	s_waitcnt lgkmcnt(6)
	s_nop 0
	v_cndmask_b32_e32 v150, 0, v150, vcc
	v_cmp_lt_u32_e32 vcc, s40, v148
	s_waitcnt lgkmcnt(5)
	s_nop 0
	v_cndmask_b32_e32 v151, 0, v151, vcc
	v_cmp_lt_u32_e32 vcc, s31, v148
	s_waitcnt lgkmcnt(4)
	s_nop 0
	v_cndmask_b32_e32 v152, 0, v152, vcc
	v_cmp_lt_u32_e32 vcc, s41, v148
	s_waitcnt lgkmcnt(3)
	s_nop 0
	v_cndmask_b32_e32 v153, 0, v153, vcc
	v_cmp_lt_u32_e32 vcc, s42, v148
	s_waitcnt lgkmcnt(2)
	s_nop 0
	v_cndmask_b32_e32 v154, 0, v154, vcc
	v_cmp_lt_u32_e32 vcc, s43, v148
	s_waitcnt lgkmcnt(1)
	s_nop 0
	v_cndmask_b32_e32 v155, 0, v155, vcc
	v_cmp_lt_u32_e32 vcc, s65, v148
	s_waitcnt lgkmcnt(0)
	s_nop 0
	v_cndmask_b32_e32 v156, 0, v156, vcc
	ds_read_b32 v157, v8 offset:11264
	ds_read_b32 v158, v8 offset:11520
	ds_read_b32 v159, v8 offset:11776
	ds_read_b32 v160, v8 offset:12032
	ds_read_b32 v161, v8 offset:12288
	ds_read_b32 v162, v8 offset:12544
	ds_read_b32 v163, v8 offset:12800
	ds_read_b32 v164, v8 offset:13056
	ds_read_b32 v165, v8 offset:13312
	ds_read_b32 v166, v8 offset:13568
	ds_read_b32 v167, v8 offset:13824
	ds_read_b32 v168, v8 offset:14080
	v_cmp_lt_u32_e32 vcc, s49, v148
	s_waitcnt lgkmcnt(11)
	s_nop 0
	v_cndmask_b32_e32 v157, 0, v157, vcc
	v_cmp_lt_u32_e32 vcc, s53, v148
	s_waitcnt lgkmcnt(10)
	s_nop 0
	v_cndmask_b32_e32 v158, 0, v158, vcc
	v_cmp_lt_u32_e32 vcc, s54, v148
	s_waitcnt lgkmcnt(9)
	s_nop 0
	v_cndmask_b32_e32 v159, 0, v159, vcc
	v_cmp_lt_u32_e32 vcc, s55, v148
	s_waitcnt lgkmcnt(8)
	s_nop 0
	v_cndmask_b32_e32 v160, 0, v160, vcc
	v_cmp_lt_u32_e32 vcc, s56, v148
	s_waitcnt lgkmcnt(7)
	s_nop 0
	v_cndmask_b32_e32 v161, 0, v161, vcc
	v_cmp_lt_u32_e32 vcc, s57, v148
	s_waitcnt lgkmcnt(6)
	s_nop 0
	v_cndmask_b32_e32 v162, 0, v162, vcc
	v_cmp_lt_u32_e32 vcc, s58, v148
	s_waitcnt lgkmcnt(5)
	s_nop 0
	v_cndmask_b32_e32 v163, 0, v163, vcc
	v_cmp_lt_u32_e32 vcc, s67, v148
	s_waitcnt lgkmcnt(4)
	s_nop 0
	v_cndmask_b32_e32 v164, 0, v164, vcc
	v_cmp_lt_u32_e32 vcc, s59, v148
	s_waitcnt lgkmcnt(3)
	s_nop 0
	v_cndmask_b32_e32 v165, 0, v165, vcc
	v_cmp_lt_u32_e32 vcc, s60, v148
	s_waitcnt lgkmcnt(2)
	s_nop 0
	v_cndmask_b32_e32 v166, 0, v166, vcc
	v_cmp_lt_u32_e32 vcc, s61, v148
	s_waitcnt lgkmcnt(1)
	s_nop 0
	v_cndmask_b32_e32 v167, 0, v167, vcc
	v_cmp_lt_u32_e32 vcc, s34, v148
	s_waitcnt lgkmcnt(0)
	s_nop 0
	v_cndmask_b32_e32 v148, 0, v168, vcc
	s_branch .Lpadskip_p5
	s_nop 0
	s_nop 0
	s_nop 0
	s_nop 0
	s_nop 0
	s_nop 0
	s_nop 0
	s_nop 0
	s_nop 0
	s_nop 0
	s_nop 0
	s_nop 0
	s_nop 0
	s_nop 0
.Lpadskip_p5:
	s_cmp_lt_i32 s16, 0
	s_cbranch_scc1 .LBB0_545
